# baseline (speedup 1.0000x reference)
.Lk1_nowarm9:
	buffer_load_dword v8, v1, s[8:11], s40 offen nt
	buffer_load_dword v9, v1, s[8:11], s41 offen nt
	buffer_load_dword v10, v1, s[8:11], s42 offen nt
	buffer_load_dword v11, v1, s[8:11], s43 offen nt
	buffer_load_dword v12, v1, s[8:11], s44 offen nt
	buffer_load_dword v13, v1, s[8:11], s45 offen nt
	buffer_load_dword v14, v1, s[8:11], s46 offen nt
	buffer_load_dword v15, v1, s[8:11], s47 offen nt
	buffer_load_dword v16, v1, s[8:11], s48 offen nt
	buffer_load_dword v17, v1, s[8:11], s49 offen nt
	buffer_load_dword v18, v1, s[8:11], s50 offen nt
	buffer_load_dword v19, v1, s[8:11], s51 offen nt
	buffer_load_dword v20, v1, s[8:11], s52 offen nt
	buffer_load_dword v21, v1, s[8:11], s53 offen nt
	buffer_load_dword v22, v1, s[8:11], s54 offen nt
	buffer_load_dword v23, v1, s[8:11], s55 offen nt
	s_add_u32 s8, s8, 0x4e200
	s_addc_u32 s9, s9, 0
	buffer_load_dword v24, v1, s[8:11], s40 offen nt
	buffer_load_dword v25, v1, s[8:11], s41 offen nt
	buffer_load_dword v26, v1, s[8:11], s42 offen nt
	buffer_load_dword v27, v1, s[8:11], s43 offen nt
	buffer_load_dword v28, v1, s[8:11], s44 offen nt
	buffer_load_dword v29, v1, s[8:11], s45 offen nt
	buffer_load_dword v30, v1, s[8:11], s46 offen nt
	buffer_load_dword v31, v1, s[8:11], s47 offen nt
	buffer_load_dword v32, v1, s[8:11], s48 offen nt
	buffer_load_dword v33, v1, s[8:11], s49 offen nt
	buffer_load_dword v34, v1, s[8:11], s50 offen nt
	buffer_load_dword v35, v1, s[8:11], s51 offen nt
	buffer_load_dword v36, v1, s[8:11], s52 offen nt
	buffer_load_dword v37, v1, s[8:11], s53 offen nt
	buffer_load_dword v38, v1, s[8:11], s54 offen nt
	buffer_load_dword v39, v1, s[8:11], s55 offen nt
	s_add_u32 s8, s8, 0x4e200
	s_addc_u32 s9, s9, 0
	buffer_load_dword v40, v1, s[8:11], s40 offen nt
	buffer_load_dword v41, v1, s[8:11], s41 offen nt
	buffer_load_dword v42, v1, s[8:11], s42 offen nt
	buffer_load_dword v43, v1, s[8:11], s43 offen nt
	buffer_load_dword v44, v1, s[8:11], s44 offen nt
	buffer_load_dword v45, v1, s[8:11], s45 offen nt
	buffer_load_dword v46, v1, s[8:11], s46 offen nt
	buffer_load_dword v47, v1, s[8:11], s47 offen nt
	buffer_load_dword v48, v1, s[8:11], s48 offen nt
	buffer_load_dword v49, v1, s[8:11], s49 offen nt
	buffer_load_dword v50, v1, s[8:11], s50 offen nt
	buffer_load_dword v51, v1, s[8:11], s51 offen nt
	buffer_load_dword v52, v1, s[8:11], s52 offen nt
	buffer_load_dword v53, v1, s[8:11], s53 offen nt
	buffer_load_dword v54, v1, s[8:11], s54 offen nt
	buffer_load_dword v55, v1, s[8:11], s55 offen nt
	s_add_u32 s8, s8, 0x4e200
	s_addc_u32 s9, s9, 0
	buffer_load_dword v56, v1, s[8:11], s40 offen nt
	buffer_load_dword v57, v1, s[8:11], s41 offen nt
	buffer_load_dword v58, v1, s[8:11], s42 offen nt
	buffer_load_dword v59, v1, s[8:11], s43 offen nt
	buffer_load_dword v60, v1, s[8:11], s44 offen nt
	buffer_load_dword v61, v1, s[8:11], s45 offen nt
	buffer_load_dword v62, v1, s[8:11], s46 offen nt
	buffer_load_dword v63, v1, s[8:11], s47 offen nt
	buffer_load_dword v64, v1, s[8:11], s48 offen nt
	buffer_load_dword v65, v1, s[8:11], s49 offen nt
	buffer_load_dword v66, v1, s[8:11], s50 offen nt
	v_mul_u32_u24_e32 v3, 0x147b, v2
	v_lshrrev_b32_e32 v3, 19, v3
	v_mul_u32_u24_e32 v98, 0x64, v3
	v_sub_u32_e32 v98, v2, v98
	v_add_u32_e32 v3, -1, v3
	v_add_u32_e32 v98, -1, v98
	s_movk_i32 s17, 0x62
	v_cmp_gt_u32_e64 s[36:37], 48, v3
	v_cmp_gt_u32_e64 s[38:39], s17, v98
	s_mul_i32 s17, s15, 0x1388
	v_add_lshl_u32 v98, v2, s17, 3
	s_and_b64 s[36:37], s[36:37], s[38:39]
	s_waitcnt vmcnt(55)
	buffer_load_dword v67, v1, s[8:11], s51 offen nt
	buffer_load_dword v68, v1, s[8:11], s52 offen nt
	buffer_load_dword v69, v1, s[8:11], s53 offen nt
	buffer_load_dword v70, v1, s[8:11], s54 offen nt
	buffer_load_dword v71, v1, s[8:11], s55 offen nt
	s_add_u32 s8, s8, 0x4e200
	s_addc_u32 s9, s9, 0
	buffer_load_dword v72, v1, s[8:11], s40 offen nt
	s_waitcnt vmcnt(49)
	v_max3_f32 v76, v8, v9, v10
	v_max3_f32 v76, v76, v11, v12
	v_max3_f32 v76, v76, v13, v14
	v_max3_f32 v76, v76, v15, v16
	v_max3_f32 v76, v76, v17, v18
	v_max3_f32 v76, v76, v19, v20
	v_max3_f32 v76, v76, v21, v22
	v_max_f32_e32 v76, v76, v23
	v_pk_add_f32 v[8:9], v[8:9], v[76:77] op_sel_hi:[1,0] neg_lo:[0,1] neg_hi:[0,1]
	v_pk_add_f32 v[10:11], v[10:11], v[76:77] op_sel_hi:[1,0] neg_lo:[0,1] neg_hi:[0,1]
	v_pk_add_f32 v[12:13], v[12:13], v[76:77] op_sel_hi:[1,0] neg_lo:[0,1] neg_hi:[0,1]
	v_pk_add_f32 v[14:15], v[14:15], v[76:77] op_sel_hi:[1,0] neg_lo:[0,1] neg_hi:[0,1]
	v_pk_add_f32 v[16:17], v[16:17], v[76:77] op_sel_hi:[1,0] neg_lo:[0,1] neg_hi:[0,1]
	v_pk_add_f32 v[18:19], v[18:19], v[76:77] op_sel_hi:[1,0] neg_lo:[0,1] neg_hi:[0,1]
	v_pk_add_f32 v[20:21], v[20:21], v[76:77] op_sel_hi:[1,0] neg_lo:[0,1] neg_hi:[0,1]
	v_pk_add_f32 v[22:23], v[22:23], v[76:77] op_sel_hi:[1,0] neg_lo:[0,1] neg_hi:[0,1]
	v_or_b32_e32 v81, 0, v8
	v_or_b32_e32 v82, 1, v9
	v_min_u32_e32 v80, v81, v82
	v_or_b32_e32 v81, 2, v10
	v_or_b32_e32 v82, 3, v11
	v_min3_u32 v80, v80, v81, v82
	v_or_b32_e32 v81, 4, v12
	v_or_b32_e32 v82, 5, v13
	v_min3_u32 v80, v80, v81, v82
	v_or_b32_e32 v81, 6, v14
	v_or_b32_e32 v82, 7, v15
	v_min3_u32 v80, v80, v81, v82
	v_or_b32_e32 v81, 8, v16
	v_or_b32_e32 v82, 9, v17
	v_min3_u32 v80, v80, v81, v82
	v_or_b32_e32 v81, 10, v18
	v_or_b32_e32 v82, 11, v19
	v_min3_u32 v80, v80, v81, v82
	v_or_b32_e32 v81, 12, v20
	v_or_b32_e32 v82, 13, v21
	v_min3_u32 v80, v80, v81, v82
	v_or_b32_e32 v81, 14, v22
	v_or_b32_e32 v82, 15, v23
	v_min3_u32 v80, v80, v81, v82
	v_pk_mul_f32 v[8:9], v[8:9], s[14:15] op_sel_hi:[1,0]
	v_pk_mul_f32 v[10:11], v[10:11], s[14:15] op_sel_hi:[1,0]
	v_pk_mul_f32 v[12:13], v[12:13], s[14:15] op_sel_hi:[1,0]
	v_pk_mul_f32 v[14:15], v[14:15], s[14:15] op_sel_hi:[1,0]
	v_pk_mul_f32 v[16:17], v[16:17], s[14:15] op_sel_hi:[1,0]
	v_pk_mul_f32 v[18:19], v[18:19], s[14:15] op_sel_hi:[1,0]
	v_pk_mul_f32 v[20:21], v[20:21], s[14:15] op_sel_hi:[1,0]
	v_pk_mul_f32 v[22:23], v[22:23], s[14:15] op_sel_hi:[1,0]
	v_exp_f32_e32 v8, v8
	v_exp_f32_e32 v9, v9
	v_exp_f32_e32 v10, v10
	v_exp_f32_e32 v11, v11
	v_exp_f32_e32 v12, v12
	v_exp_f32_e32 v13, v13
	v_exp_f32_e32 v14, v14
	v_exp_f32_e32 v15, v15
	v_exp_f32_e32 v16, v16
	v_exp_f32_e32 v17, v17
	v_exp_f32_e32 v18, v18
	v_exp_f32_e32 v19, v19
	v_exp_f32_e32 v20, v20
	v_exp_f32_e32 v21, v21
	v_exp_f32_e32 v22, v22
	v_exp_f32_e32 v23, v23
	v_pk_add_f32 v[78:79], v[8:9], v[10:11]
	v_pk_add_f32 v[78:79], v[78:79], v[12:13]
	v_pk_add_f32 v[78:79], v[78:79], v[14:15]
	v_pk_add_f32 v[78:79], v[78:79], v[16:17]
	v_pk_add_f32 v[78:79], v[78:79], v[18:19]
	v_pk_add_f32 v[78:79], v[78:79], v[20:21]
	v_pk_add_f32 v[78:79], v[78:79], v[22:23]
	v_add_f32_e32 v78, v78, v79
	v_cvt_f64_f32_e32 v[86:87], v78
	v_mov_b32_e32 v75, v80
	v_mov_b32_e32 v73, v76
	s_waitcnt vmcnt(33)
	v_max3_f32 v76, v24, v25, v26
	v_max3_f32 v76, v76, v27, v28
	v_max3_f32 v76, v76, v29, v30
	v_max3_f32 v76, v76, v31, v32
	v_max3_f32 v76, v76, v33, v34
	v_max3_f32 v76, v76, v35, v36
	v_max3_f32 v76, v76, v37, v38
	v_max_f32_e32 v76, v76, v39
	v_max_f32_e32 v100, v73, v76
	v_cmp_gt_f32_e64 s[26:27], v76, v73
	v_sub_f32_e32 v83, v73, v100
	v_mul_f32_e32 v83, s14, v83
	v_exp_f32_e32 v83, v83
	v_pk_add_f32 v[24:25], v[24:25], v[100:101] op_sel_hi:[1,0] neg_lo:[0,1] neg_hi:[0,1]
	v_pk_add_f32 v[26:27], v[26:27], v[100:101] op_sel_hi:[1,0] neg_lo:[0,1] neg_hi:[0,1]
	v_pk_add_f32 v[28:29], v[28:29], v[100:101] op_sel_hi:[1,0] neg_lo:[0,1] neg_hi:[0,1]
	v_pk_add_f32 v[30:31], v[30:31], v[100:101] op_sel_hi:[1,0] neg_lo:[0,1] neg_hi:[0,1]
	v_pk_add_f32 v[32:33], v[32:33], v[100:101] op_sel_hi:[1,0] neg_lo:[0,1] neg_hi:[0,1]
	v_pk_add_f32 v[34:35], v[34:35], v[100:101] op_sel_hi:[1,0] neg_lo:[0,1] neg_hi:[0,1]
	v_pk_add_f32 v[36:37], v[36:37], v[100:101] op_sel_hi:[1,0] neg_lo:[0,1] neg_hi:[0,1]
	v_pk_add_f32 v[38:39], v[38:39], v[100:101] op_sel_hi:[1,0] neg_lo:[0,1] neg_hi:[0,1]
	v_cvt_f64_f32_e32 v[90:91], v83
	v_or_b32_e32 v81, 16, v24
	v_or_b32_e32 v82, 17, v25
	v_min_u32_e32 v80, v81, v82
	v_or_b32_e32 v81, 18, v26
	v_or_b32_e32 v82, 19, v27
	v_min3_u32 v80, v80, v81, v82
	v_or_b32_e32 v81, 20, v28
	v_or_b32_e32 v82, 21, v29
	v_min3_u32 v80, v80, v81, v82
	v_or_b32_e32 v81, 22, v30
	v_or_b32_e32 v82, 23, v31
	v_min3_u32 v80, v80, v81, v82
	v_or_b32_e32 v81, 24, v32
	v_or_b32_e32 v82, 25, v33
	v_min3_u32 v80, v80, v81, v82
	v_or_b32_e32 v81, 26, v34
	v_or_b32_e32 v82, 27, v35
	v_min3_u32 v80, v80, v81, v82
	v_or_b32_e32 v81, 28, v36
	v_or_b32_e32 v82, 29, v37
	v_min3_u32 v80, v80, v81, v82
	v_or_b32_e32 v81, 30, v38
	v_or_b32_e32 v82, 31, v39
	v_min3_u32 v80, v80, v81, v82
	v_pk_mul_f32 v[24:25], v[24:25], s[14:15] op_sel_hi:[1,0]
	v_pk_mul_f32 v[26:27], v[26:27], s[14:15] op_sel_hi:[1,0]
	v_pk_mul_f32 v[28:29], v[28:29], s[14:15] op_sel_hi:[1,0]
	v_pk_mul_f32 v[30:31], v[30:31], s[14:15] op_sel_hi:[1,0]
	v_pk_mul_f32 v[32:33], v[32:33], s[14:15] op_sel_hi:[1,0]
	v_pk_mul_f32 v[34:35], v[34:35], s[14:15] op_sel_hi:[1,0]
	v_pk_mul_f32 v[36:37], v[36:37], s[14:15] op_sel_hi:[1,0]
	v_pk_mul_f32 v[38:39], v[38:39], s[14:15] op_sel_hi:[1,0]
	v_exp_f32_e32 v24, v24
	v_exp_f32_e32 v25, v25
	v_exp_f32_e32 v26, v26
	v_exp_f32_e32 v27, v27
	v_exp_f32_e32 v28, v28
	v_exp_f32_e32 v29, v29
	v_exp_f32_e32 v30, v30
	v_exp_f32_e32 v31, v31
	v_exp_f32_e32 v32, v32
	v_exp_f32_e32 v33, v33
	v_exp_f32_e32 v34, v34
	v_exp_f32_e32 v35, v35
	v_exp_f32_e32 v36, v36
	v_exp_f32_e32 v37, v37
	v_exp_f32_e32 v38, v38
	v_exp_f32_e32 v39, v39
	v_pk_add_f32 v[78:79], v[24:25], v[26:27]
	v_pk_add_f32 v[78:79], v[78:79], v[28:29]
	v_pk_add_f32 v[78:79], v[78:79], v[30:31]
	v_pk_add_f32 v[78:79], v[78:79], v[32:33]
	v_pk_add_f32 v[78:79], v[78:79], v[34:35]
	v_pk_add_f32 v[78:79], v[78:79], v[36:37]
	v_pk_add_f32 v[78:79], v[78:79], v[38:39]
	v_add_f32_e32 v78, v78, v79
	v_cvt_f64_f32_e32 v[84:85], v78
	v_cndmask_b32_e64 v75, v75, v80, s[26:27]
	v_mov_b32_e32 v73, v100
	v_fma_f64 v[86:87], v[86:87], v[90:91], v[84:85]
	s_waitcnt vmcnt(17)
	v_max3_f32 v76, v40, v41, v42
	v_max3_f32 v76, v76, v43, v44
	v_max3_f32 v76, v76, v45, v46
	v_max3_f32 v76, v76, v47, v48
	v_max3_f32 v76, v76, v49, v50
	v_max3_f32 v76, v76, v51, v52
	v_max3_f32 v76, v76, v53, v54
	v_max_f32_e32 v76, v76, v55
	v_max_f32_e32 v100, v73, v76
	v_cmp_gt_f32_e64 s[26:27], v76, v73
	v_sub_f32_e32 v83, v73, v100
	v_mul_f32_e32 v83, s14, v83
	v_exp_f32_e32 v83, v83
	v_pk_add_f32 v[40:41], v[40:41], v[100:101] op_sel_hi:[1,0] neg_lo:[0,1] neg_hi:[0,1]
	v_pk_add_f32 v[42:43], v[42:43], v[100:101] op_sel_hi:[1,0] neg_lo:[0,1] neg_hi:[0,1]
	v_pk_add_f32 v[44:45], v[44:45], v[100:101] op_sel_hi:[1,0] neg_lo:[0,1] neg_hi:[0,1]
	v_pk_add_f32 v[46:47], v[46:47], v[100:101] op_sel_hi:[1,0] neg_lo:[0,1] neg_hi:[0,1]
	v_pk_add_f32 v[48:49], v[48:49], v[100:101] op_sel_hi:[1,0] neg_lo:[0,1] neg_hi:[0,1]
	v_pk_add_f32 v[50:51], v[50:51], v[100:101] op_sel_hi:[1,0] neg_lo:[0,1] neg_hi:[0,1]
	v_pk_add_f32 v[52:53], v[52:53], v[100:101] op_sel_hi:[1,0] neg_lo:[0,1] neg_hi:[0,1]
	v_pk_add_f32 v[54:55], v[54:55], v[100:101] op_sel_hi:[1,0] neg_lo:[0,1] neg_hi:[0,1]
	v_cvt_f64_f32_e32 v[90:91], v83
	v_or_b32_e32 v81, 32, v40
	v_or_b32_e32 v82, 33, v41
	v_min_u32_e32 v80, v81, v82
	v_or_b32_e32 v81, 34, v42
	v_or_b32_e32 v82, 35, v43
	v_min3_u32 v80, v80, v81, v82
	v_or_b32_e32 v81, 36, v44
	v_or_b32_e32 v82, 37, v45
	v_min3_u32 v80, v80, v81, v82
	v_or_b32_e32 v81, 38, v46
	v_or_b32_e32 v82, 39, v47
	v_min3_u32 v80, v80, v81, v82
	v_or_b32_e32 v81, 40, v48
	v_or_b32_e32 v82, 41, v49
	v_min3_u32 v80, v80, v81, v82
	v_or_b32_e32 v81, 42, v50
	v_or_b32_e32 v82, 43, v51
	v_min3_u32 v80, v80, v81, v82
	v_or_b32_e32 v81, 44, v52
	v_or_b32_e32 v82, 45, v53
	v_min3_u32 v80, v80, v81, v82
	v_or_b32_e32 v81, 46, v54
	v_or_b32_e32 v82, 47, v55
	v_min3_u32 v80, v80, v81, v82
	v_pk_mul_f32 v[40:41], v[40:41], s[14:15] op_sel_hi:[1,0]
	v_pk_mul_f32 v[42:43], v[42:43], s[14:15] op_sel_hi:[1,0]
	v_pk_mul_f32 v[44:45], v[44:45], s[14:15] op_sel_hi:[1,0]
	v_pk_mul_f32 v[46:47], v[46:47], s[14:15] op_sel_hi:[1,0]
	v_pk_mul_f32 v[48:49], v[48:49], s[14:15] op_sel_hi:[1,0]
	v_pk_mul_f32 v[50:51], v[50:51], s[14:15] op_sel_hi:[1,0]
	v_pk_mul_f32 v[52:53], v[52:53], s[14:15] op_sel_hi:[1,0]
	v_pk_mul_f32 v[54:55], v[54:55], s[14:15] op_sel_hi:[1,0]
	v_exp_f32_e32 v40, v40
	v_exp_f32_e32 v41, v41
	v_exp_f32_e32 v42, v42
	v_exp_f32_e32 v43, v43
	v_exp_f32_e32 v44, v44
	v_exp_f32_e32 v45, v45
	v_exp_f32_e32 v46, v46
	v_exp_f32_e32 v47, v47
	v_exp_f32_e32 v48, v48
	v_exp_f32_e32 v49, v49
	v_exp_f32_e32 v50, v50
	v_exp_f32_e32 v51, v51
	v_exp_f32_e32 v52, v52
	v_exp_f32_e32 v53, v53
	v_exp_f32_e32 v54, v54
	v_exp_f32_e32 v55, v55
	v_pk_add_f32 v[78:79], v[40:41], v[42:43]
	v_pk_add_f32 v[78:79], v[78:79], v[44:45]
	v_pk_add_f32 v[78:79], v[78:79], v[46:47]
	v_pk_add_f32 v[78:79], v[78:79], v[48:49]
	v_pk_add_f32 v[78:79], v[78:79], v[50:51]
	v_pk_add_f32 v[78:79], v[78:79], v[52:53]
	v_pk_add_f32 v[78:79], v[78:79], v[54:55]
	v_add_f32_e32 v78, v78, v79
	v_cvt_f64_f32_e32 v[84:85], v78
	v_cndmask_b32_e64 v75, v75, v80, s[26:27]
	v_mov_b32_e32 v73, v100
	v_fma_f64 v[86:87], v[86:87], v[90:91], v[84:85]
	s_waitcnt vmcnt(9)
	v_max3_f32 v76, v56, v57, v58
	v_max3_f32 v76, v76, v59, v60
	v_max3_f32 v76, v76, v61, v62
	v_max_f32_e32 v76, v76, v63
	v_max_f32_e32 v100, v73, v76
	v_cmp_gt_f32_e64 s[26:27], v76, v73
	v_sub_f32_e32 v83, v73, v100
	v_mul_f32_e32 v83, s14, v83
	v_exp_f32_e32 v83, v83
	v_pk_add_f32 v[56:57], v[56:57], v[100:101] op_sel_hi:[1,0] neg_lo:[0,1] neg_hi:[0,1]
	v_pk_add_f32 v[58:59], v[58:59], v[100:101] op_sel_hi:[1,0] neg_lo:[0,1] neg_hi:[0,1]
	v_pk_add_f32 v[60:61], v[60:61], v[100:101] op_sel_hi:[1,0] neg_lo:[0,1] neg_hi:[0,1]
	v_pk_add_f32 v[62:63], v[62:63], v[100:101] op_sel_hi:[1,0] neg_lo:[0,1] neg_hi:[0,1]
	v_cvt_f64_f32_e32 v[90:91], v83
	v_or_b32_e32 v81, 48, v56
	v_or_b32_e32 v82, 49, v57
	v_min_u32_e32 v80, v81, v82
	v_or_b32_e32 v81, 50, v58
	v_or_b32_e32 v82, 51, v59
	v_min3_u32 v80, v80, v81, v82
	v_or_b32_e32 v81, 52, v60
	v_or_b32_e32 v82, 53, v61
	v_min3_u32 v80, v80, v81, v82
	v_or_b32_e32 v81, 54, v62
	v_or_b32_e32 v82, 55, v63
	v_min3_u32 v80, v80, v81, v82
	v_pk_mul_f32 v[56:57], v[56:57], s[14:15] op_sel_hi:[1,0]
	v_pk_mul_f32 v[58:59], v[58:59], s[14:15] op_sel_hi:[1,0]
	v_pk_mul_f32 v[60:61], v[60:61], s[14:15] op_sel_hi:[1,0]
	v_pk_mul_f32 v[62:63], v[62:63], s[14:15] op_sel_hi:[1,0]
	v_exp_f32_e32 v56, v56
	v_exp_f32_e32 v57, v57
	v_exp_f32_e32 v58, v58
	v_exp_f32_e32 v59, v59
	v_exp_f32_e32 v60, v60
	v_exp_f32_e32 v61, v61
	v_exp_f32_e32 v62, v62
	v_exp_f32_e32 v63, v63
	v_pk_add_f32 v[78:79], v[56:57], v[58:59]
	v_pk_add_f32 v[78:79], v[78:79], v[60:61]
	v_pk_add_f32 v[78:79], v[78:79], v[62:63]
	v_add_f32_e32 v78, v78, v79
	v_cvt_f64_f32_e32 v[84:85], v78
	v_cndmask_b32_e64 v75, v75, v80, s[26:27]
	v_mov_b32_e32 v73, v100
	v_fma_f64 v[86:87], v[86:87], v[90:91], v[84:85]
	s_waitcnt vmcnt(5)
	v_max3_f32 v76, v64, v65, v66
	v_max_f32_e32 v76, v76, v67
	v_max_f32_e32 v100, v73, v76
	v_cmp_gt_f32_e64 s[26:27], v76, v73
	v_sub_f32_e32 v83, v73, v100
	v_mul_f32_e32 v83, s14, v83
	v_exp_f32_e32 v83, v83
	v_pk_add_f32 v[64:65], v[64:65], v[100:101] op_sel_hi:[1,0] neg_lo:[0,1] neg_hi:[0,1]
	v_pk_add_f32 v[66:67], v[66:67], v[100:101] op_sel_hi:[1,0] neg_lo:[0,1] neg_hi:[0,1]
	v_cvt_f64_f32_e32 v[90:91], v83
	v_or_b32_e32 v81, 56, v64
	v_or_b32_e32 v82, 57, v65
	v_min_u32_e32 v80, v81, v82
	v_or_b32_e32 v81, 58, v66
	v_or_b32_e32 v82, 59, v67
	v_min3_u32 v80, v80, v81, v82
	v_pk_mul_f32 v[64:65], v[64:65], s[14:15] op_sel_hi:[1,0]
	v_pk_mul_f32 v[66:67], v[66:67], s[14:15] op_sel_hi:[1,0]
	v_exp_f32_e32 v64, v64
	v_exp_f32_e32 v65, v65
	v_exp_f32_e32 v66, v66
	v_exp_f32_e32 v67, v67
	s_nop 0
	v_pk_add_f32 v[78:79], v[64:65], v[66:67]
	v_add_f32_e32 v78, v78, v79
	v_cvt_f64_f32_e32 v[84:85], v78
	v_cndmask_b32_e64 v75, v75, v80, s[26:27]
	v_mov_b32_e32 v73, v100
	v_fma_f64 v[86:87], v[86:87], v[90:91], v[84:85]
	s_waitcnt vmcnt(4)
	v_max_f32_e32 v100, v73, v68
	v_cmp_gt_f32_e64 s[26:27], v68, v73
	v_sub_f32_e32 v83, v73, v100
	v_sub_f32_e32 v68, v68, v100
	v_mul_f32_e32 v83, s14, v83
	v_mul_f32_e32 v68, s14, v68
	v_exp_f32_e32 v83, v83
	v_exp_f32_e32 v68, v68
	v_cndmask_b32_e64 v75, v75, 60, s[26:27]
	v_cvt_f64_f32_e32 v[84:85], v83
	v_cvt_f64_f32_e32 v[90:91], v68
	v_mov_b32_e32 v73, v100
	v_fma_f64 v[86:87], v[86:87], v[84:85], v[90:91]
	s_waitcnt vmcnt(3)
	v_max_f32_e32 v100, v73, v69
	v_cmp_gt_f32_e64 s[26:27], v69, v73
	v_sub_f32_e32 v83, v73, v100
	v_sub_f32_e32 v69, v69, v100
	v_mul_f32_e32 v83, s14, v83
	v_mul_f32_e32 v69, s14, v69
	v_exp_f32_e32 v83, v83
	v_exp_f32_e32 v69, v69
	v_cndmask_b32_e64 v75, v75, 61, s[26:27]
	v_cvt_f64_f32_e32 v[84:85], v83
	v_cvt_f64_f32_e32 v[90:91], v69
	v_mov_b32_e32 v73, v100
	v_fma_f64 v[86:87], v[86:87], v[84:85], v[90:91]
	s_waitcnt vmcnt(2)
	v_max_f32_e32 v100, v73, v70
	v_cmp_gt_f32_e64 s[26:27], v70, v73
	v_sub_f32_e32 v83, v73, v100
	v_sub_f32_e32 v70, v70, v100
	v_mul_f32_e32 v83, s14, v83
	v_mul_f32_e32 v70, s14, v70
	v_exp_f32_e32 v83, v83
	v_exp_f32_e32 v70, v70
	v_cndmask_b32_e64 v75, v75, 62, s[26:27]
	v_cvt_f64_f32_e32 v[84:85], v83
	v_cvt_f64_f32_e32 v[90:91], v70
	v_mov_b32_e32 v73, v100
	v_fma_f64 v[86:87], v[86:87], v[84:85], v[90:91]
	s_waitcnt vmcnt(1)
	v_max_f32_e32 v100, v73, v71
	v_cmp_gt_f32_e64 s[26:27], v71, v73
	v_sub_f32_e32 v83, v73, v100
	v_sub_f32_e32 v71, v71, v100
	v_mul_f32_e32 v83, s14, v83
	v_mul_f32_e32 v71, s14, v71
	v_exp_f32_e32 v83, v83
	v_exp_f32_e32 v71, v71
	v_cndmask_b32_e64 v75, v75, 63, s[26:27]
	v_cvt_f64_f32_e32 v[84:85], v83
	v_cvt_f64_f32_e32 v[90:91], v71
	v_mov_b32_e32 v73, v100
	v_fma_f64 v[86:87], v[86:87], v[84:85], v[90:91]
	s_waitcnt vmcnt(0)
	v_max_f32_e32 v100, v73, v72
	v_cmp_gt_f32_e64 s[26:27], v72, v73
	v_sub_f32_e32 v83, v73, v100
	v_sub_f32_e32 v72, v72, v100
	v_mul_f32_e32 v83, s14, v83
	v_mul_f32_e32 v72, s14, v72
	v_exp_f32_e32 v83, v83
	v_exp_f32_e32 v72, v72
	v_cndmask_b32_e64 v75, v75, 64, s[26:27]
	v_cvt_f64_f32_e32 v[84:85], v83
	v_cvt_f64_f32_e32 v[90:91], v72
	v_fma_f64 v[86:87], v[86:87], v[84:85], v[90:91]
	v_rcp_f64_e32 v[88:89], v[86:87]
	v_cmp_gt_u32_e32 vcc, 64, v75
	s_and_b64 vcc, vcc, s[36:37]
	v_fma_f64 v[90:91], -v[86:87], v[88:89], 1.0
	v_fma_f64 v[88:89], v[90:91], v[88:89], v[88:89]
	v_cvt_f32_f64_e32 v3, v[88:89]
	v_cndmask_b32_e32 v74, 0, v3, vcc
	global_store_dwordx2 v98, v[74:75], s[6:7]
